# baseline (speedup 1.0000x reference)
.LBB7_5:
	s_add_i32 s10, s11, s8
	s_cmpk_gt_i32 s5, 0x4ff
	s_cselect_b64 s[4:5], -1, 0
	s_and_b64 s[4:5], exec, s[4:5]
	s_mov_b64 vcc, s[4:5]
	s_cbranch_vccz .LBB7_7
	s_lshl_b32 s8, s33, 1
	s_abs_i32 s9, s8
	v_cvt_f32_u32_e32 v1, s9
	s_sub_i32 s13, 0, s9
	s_abs_i32 s11, s10
	s_xor_b32 s12, s10, s8
	v_rcp_iflag_f32_e32 v1, v1
	s_ashr_i32 s12, s12, 31
	v_mul_f32_e32 v1, 0x4f7ffffe, v1
	v_cvt_u32_f32_e32 v1, v1
	s_nop 0
	v_readfirstlane_b32 s14, v1
	s_mul_i32 s13, s13, s14
	s_mul_hi_u32 s13, s14, s13
	s_add_i32 s14, s14, s13
	s_mul_hi_u32 s13, s11, s14
	s_mul_i32 s14, s13, s9
	s_sub_i32 s11, s11, s14
	s_add_i32 s15, s13, 1
	s_sub_i32 s14, s11, s9
	s_cmp_ge_u32 s11, s9
	s_cselect_b32 s13, s15, s13
	s_cselect_b32 s11, s14, s11
	s_add_i32 s14, s13, 1
	s_cmp_ge_u32 s11, s9
	s_cselect_b32 s9, s14, s13
	s_xor_b32 s9, s9, s12
	s_sub_i32 s9, s9, s12
	s_lshl_b32 s11, s9, 1
	s_sub_i32 s12, s3, s11
	s_min_i32 s12, s12, 2
	s_abs_i32 s13, s12
	v_cvt_f32_u32_e32 v1, s13
	s_sub_i32 s15, 0, s13
	s_mul_i32 s9, s9, s8
	s_sub_i32 s8, s10, s9
	v_rcp_iflag_f32_e32 v1, v1
	s_abs_i32 s9, s8
	s_xor_b32 s14, s8, s12
	s_ashr_i32 s14, s14, 31
	v_mul_f32_e32 v1, 0x4f7ffffe, v1
	v_cvt_u32_f32_e32 v1, v1
	s_nop 0
	v_readfirstlane_b32 s16, v1
	s_mul_i32 s15, s15, s16
	s_mul_hi_u32 s15, s16, s15
	s_add_i32 s16, s16, s15
	s_mul_hi_u32 s15, s9, s16
	s_mul_i32 s16, s15, s13
	s_sub_i32 s9, s9, s16
	s_add_i32 s17, s15, 1
	s_sub_i32 s16, s9, s13
	s_cmp_ge_u32 s9, s13
	s_cselect_b32 s15, s17, s15
	s_cselect_b32 s9, s16, s9
	s_add_i32 s16, s15, 1
	s_cmp_ge_u32 s9, s13
	s_cselect_b32 s9, s16, s15
	s_xor_b32 s9, s9, s14
	s_sub_i32 s67, s9, s14
	s_mul_i32 s9, s67, s12
	s_sub_i32 s8, s8, s9
	s_add_i32 s12, s8, s11
	s_load_dwordx4 s[16:19], s[0:1], 0x0
	s_load_dword s11, s[0:1], 0x1c
	s_cbranch_execz .LBB7_8
	s_branch .LBB7_9

.LBB7_11:
	s_mov_b64 s[26:27], 0x80
	s_and_b32 s22, s20, 3
	s_add_i32 m0, s43, 0x18000
	v_lshl_add_u64 v[8:9], v[8:9], 0, s[26:27]
	s_lshl_b32 s48, s21, 6
	s_lshl_b32 s21, s21, 13
	s_lshl_b32 s23, s22, 12
	s_waitcnt vmcnt(4)
	s_barrier
	global_load_lds_dwordx4 v[8:9], off
	v_lshl_add_u64 v[6:7], v[6:7], 0, s[26:27]
	s_add_i32 m0, s43, 0x1a000
	s_add_i32 s49, s43, 0x8000
	s_add_i32 s50, s43, 0xa000
	global_load_lds_dwordx4 v[6:7], off
	v_lshl_add_u64 v[4:5], v[4:5], 0, s[26:27]
	s_mov_b32 m0, s49
	s_add_u32 s0, s30, 0xc080
	global_load_lds_dwordx4 v[4:5], off
	v_lshl_add_u64 v[2:3], v[2:3], 0, s[26:27]
	s_mov_b32 m0, s50
	s_addc_u32 s1, s31, 0
	global_load_lds_dwordx4 v[2:3], off
	s_add_i32 m0, s43, 0x1c000
	v_lshl_add_u64 v[2:3], s[0:1], 0, v[146:147]
	global_load_lds_dwordx4 v[2:3], off
	v_lshl_add_u64 v[2:3], s[0:1], 0, v[150:151]
	s_add_i32 m0, s43, 0x1e000
	s_lshl_b32 s53, s33, 1
	global_load_lds_dwordx4 v[2:3], off
	s_abs_i32 s54, s53
	v_cvt_f32_u32_e32 v6, s54
	v_and_b32_e32 v165, 15, v0
	v_and_b32_e32 v2, 48, v0
	v_lshlrev_b32_e32 v4, 2, v0
	v_rcp_iflag_f32_e32 v6, v6
	v_lshlrev_b32_e32 v5, 6, v0
	v_bfe_u32 v167, v0, 3, 3
	v_and_b32_e32 v0, 7, v0
	s_abs_i32 s57, s33
	v_lshlrev_b32_e32 v168, 4, v0
	v_add_lshl_u32 v169, v0, s10, 4
	v_mul_f32_e32 v0, 0x4f7ffffe, v6
	v_cvt_f32_u32_e32 v6, s57
	s_movk_i32 s0, 0x3c0
	s_mulk_i32 s20, 0x900
	v_cvt_u32_f32_e32 v0, v0
	v_rcp_iflag_f32_e32 v6, v6
	v_and_or_b32 v5, v5, s0, v2
	s_add_i32 s0, s20, 0
	v_lshl_or_b32 v3, v165, 6, v2
	v_and_b32_e32 v4, 32, v4
	s_add_i32 s0, s0, 0x20000
	v_bitop3_b32 v3, v3, s21, v4 bitop3:0xde
	v_bitop3_b32 v166, s23, v5, v4 bitop3:0xf6
	s_movk_i32 s1, 0x90
	v_mov_b32_e32 v4, s0
	v_mad_u32_u24 v5, v165, s1, v4
	v_mad_u32_u24 v4, v167, s1, v4
	v_readfirstlane_b32 s1, v0
	v_mul_f32_e32 v0, 0x4f7ffffe, v6
	v_cvt_u32_f32_e32 v0, v0
	s_sub_i32 s0, 0, s54
	s_mul_i32 s0, s0, s1
	s_mul_hi_u32 s0, s1, s0
	s_add_i32 s59, s1, s0
	s_sub_i32 s0, 0, s57
	v_readfirstlane_b32 s1, v0
	s_waitcnt vmcnt(6)
	s_mul_i32 s0, s0, s1
	v_add_u16_e32 v0, v1, v10
	s_mul_hi_u32 s0, s1, s0
	v_lshrrev_b16_e32 v0, 1, v0
	s_add_i32 s65, 0, 0x10000
	s_add_i32 s66, 0, 0x14000
	s_mov_b32 s23, 0x20000
	s_lshl_b32 s51, s22, 6
	s_waitcnt lgkmcnt(0)
	s_ashr_i32 s52, s11, 31
	s_lshl_b32 s22, s10, 17
	s_and_b32 s21, s9, 0xffff
	s_mov_b32 s20, s8
	s_lshl_b32 s55, s10, 5
	s_mul_i32 s56, s10, 48
	s_bfe_i32 s58, s33, 0x1001c
	s_ashr_i32 s60, s33, 31
	s_add_i32 s61, s1, s0
	s_mul_i32 s62, s10, 0xc0
	s_mul_i32 s63, s10, 0x60
	s_lshl_b32 s64, s10, 4
	v_add_lshl_u32 v152, v11, v0, 1
	v_mov_b32_e32 v153, v147
	v_add_lshl_u32 v154, v12, v0, 1
	v_mov_b32_e32 v155, v147
	v_mov_b64_e32 v[156:157], s[6:7]
	v_add_u32_e32 v170, s65, v166
	v_add_u32_e32 v171, 0, v3
	v_add_u32_e32 v172, s66, v166
	v_add_u32_e32 v173, v5, v2
	v_add_u32_e32 v174, v4, v168
	s_barrier

.LBB7_17:
	s_ashr_i32 s8, s34, 3
	s_add_i32 s34, s68, s8
	s_mov_b64 s[8:9], -1
	s_mov_b64 vcc, s[4:5]
	s_cbranch_vccz .LBB7_19
	s_abs_i32 s9, s34
	s_mul_hi_u32 s35, s9, s59
	s_mul_i32 s68, s35, s54
	s_ashr_i32 s8, s34, 31
	s_sub_i32 s9, s9, s68
	s_xor_b32 s8, s8, s58
	s_add_i32 s68, s35, 1
	s_sub_i32 s69, s9, s54
	s_cmp_ge_u32 s9, s54
	s_cselect_b32 s35, s68, s35
	s_cselect_b32 s9, s69, s9
	s_add_i32 s68, s35, 1
	s_cmp_ge_u32 s9, s54
	s_cselect_b32 s9, s68, s35
	s_xor_b32 s9, s9, s8
	s_sub_i32 s8, s9, s8
	s_lshl_b32 s9, s8, 1
	s_sub_i32 s35, s3, s9
	s_min_i32 s35, s35, 2
	s_abs_i32 s68, s35
	v_cvt_f32_u32_e32 v0, s68
	s_sub_i32 s72, 0, s68
	s_mul_i32 s8, s8, s53
	s_sub_i32 s8, s34, s8
	v_rcp_iflag_f32_e32 v0, v0
	s_abs_i32 s71, s8
	s_xor_b32 s69, s8, s35
	s_ashr_i32 s69, s69, 31
	v_mul_f32_e32 v0, 0x4f7ffffe, v0
	v_cvt_u32_f32_e32 v0, v0
	s_nop 0
	v_readfirstlane_b32 s73, v0
	s_mul_i32 s72, s72, s73
	s_mul_hi_u32 s72, s73, s72
	s_add_i32 s73, s73, s72
	s_mul_hi_u32 s72, s71, s73
	s_mul_i32 s73, s72, s68
	s_sub_i32 s71, s71, s73
	s_add_i32 s73, s72, 1
	s_sub_i32 s74, s71, s68
	s_cmp_ge_u32 s71, s68
	s_cselect_b32 s72, s73, s72
	s_cselect_b32 s71, s74, s71
	s_add_i32 s73, s72, 1
	s_cmp_ge_u32 s71, s68
	s_cselect_b32 s68, s73, s72
	s_xor_b32 s68, s68, s69
	s_sub_i32 s68, s68, s69
	s_mul_i32 s35, s68, s35
	s_sub_i32 s8, s8, s35
	s_add_i32 s35, s8, s9
	s_mov_b64 s[8:9], 0

.LBB9_5:
	s_add_i32 s10, s11, s8
	s_cmpk_gt_i32 s5, 0x4ff
	s_cselect_b64 s[4:5], -1, 0
	s_and_b64 s[4:5], exec, s[4:5]
	s_mov_b64 vcc, s[4:5]
	s_cbranch_vccz .LBB9_7
	s_lshl_b32 s8, s33, 1
	s_abs_i32 s9, s8
	v_cvt_f32_u32_e32 v1, s9
	s_sub_i32 s13, 0, s9
	s_abs_i32 s11, s10
	s_xor_b32 s12, s10, s8
	v_rcp_iflag_f32_e32 v1, v1
	s_ashr_i32 s12, s12, 31
	v_mul_f32_e32 v1, 0x4f7ffffe, v1
	v_cvt_u32_f32_e32 v1, v1
	s_nop 0
	v_readfirstlane_b32 s14, v1
	s_mul_i32 s13, s13, s14
	s_mul_hi_u32 s13, s14, s13
	s_add_i32 s14, s14, s13
	s_mul_hi_u32 s13, s11, s14
	s_mul_i32 s14, s13, s9
	s_sub_i32 s11, s11, s14
	s_add_i32 s15, s13, 1
	s_sub_i32 s14, s11, s9
	s_cmp_ge_u32 s11, s9
	s_cselect_b32 s13, s15, s13
	s_cselect_b32 s11, s14, s11
	s_add_i32 s14, s13, 1
	s_cmp_ge_u32 s11, s9
	s_cselect_b32 s9, s14, s13
	s_xor_b32 s9, s9, s12
	s_sub_i32 s9, s9, s12
	s_lshl_b32 s11, s9, 1
	s_sub_i32 s12, s3, s11
	s_min_i32 s12, s12, 2
	s_abs_i32 s13, s12
	v_cvt_f32_u32_e32 v1, s13
	s_sub_i32 s15, 0, s13
	s_mul_i32 s9, s9, s8
	s_sub_i32 s8, s10, s9
	v_rcp_iflag_f32_e32 v1, v1
	s_abs_i32 s9, s8
	s_xor_b32 s14, s8, s12
	s_ashr_i32 s14, s14, 31
	v_mul_f32_e32 v1, 0x4f7ffffe, v1
	v_cvt_u32_f32_e32 v1, v1
	s_nop 0
	v_readfirstlane_b32 s16, v1
	s_mul_i32 s15, s15, s16
	s_mul_hi_u32 s15, s16, s15
	s_add_i32 s16, s16, s15
	s_mul_hi_u32 s15, s9, s16
	s_mul_i32 s16, s15, s13
	s_sub_i32 s9, s9, s16
	s_add_i32 s17, s15, 1
	s_sub_i32 s16, s9, s13
	s_cmp_ge_u32 s9, s13
	s_cselect_b32 s15, s17, s15
	s_cselect_b32 s9, s16, s9
	s_add_i32 s16, s15, 1
	s_cmp_ge_u32 s9, s13
	s_cselect_b32 s9, s16, s15
	s_xor_b32 s9, s9, s14
	s_sub_i32 s68, s9, s14
	s_mul_i32 s9, s68, s12
	s_sub_i32 s8, s8, s9
	s_add_i32 s12, s8, s11
	s_load_dwordx4 s[16:19], s[0:1], 0x0
	s_load_dword s11, s[0:1], 0x1c
	s_cbranch_execz .LBB9_8
	s_branch .LBB9_9

.LBB9_11:
	s_mov_b64 s[26:27], 0x80
	s_and_b32 s22, s20, 3
	s_add_i32 m0, s43, 0x18000
	v_lshl_add_u64 v[8:9], v[8:9], 0, s[26:27]
	s_lshl_b32 s48, s21, 6
	s_lshl_b32 s21, s21, 13
	s_lshl_b32 s23, s22, 12
	s_waitcnt vmcnt(4)
	s_barrier
	global_load_lds_dwordx4 v[8:9], off
	v_lshl_add_u64 v[6:7], v[6:7], 0, s[26:27]
	s_add_i32 m0, s43, 0x1a000
	s_add_i32 s49, s43, 0x8000
	s_add_i32 s50, s43, 0xa000
	global_load_lds_dwordx4 v[6:7], off
	v_lshl_add_u64 v[4:5], v[4:5], 0, s[26:27]
	s_mov_b32 m0, s49
	s_add_u32 s0, s30, 0xc080
	global_load_lds_dwordx4 v[4:5], off
	v_lshl_add_u64 v[2:3], v[2:3], 0, s[26:27]
	s_mov_b32 m0, s50
	s_addc_u32 s1, s31, 0
	global_load_lds_dwordx4 v[2:3], off
	s_add_i32 m0, s43, 0x1c000
	v_lshl_add_u64 v[2:3], s[0:1], 0, v[146:147]
	global_load_lds_dwordx4 v[2:3], off
	v_lshl_add_u64 v[2:3], s[0:1], 0, v[150:151]
	s_add_i32 m0, s43, 0x1e000
	s_lshl_b32 s53, s33, 1
	global_load_lds_dwordx4 v[2:3], off
	s_abs_i32 s54, s53
	v_cvt_f32_u32_e32 v6, s54
	v_and_b32_e32 v167, 15, v0
	v_and_b32_e32 v2, 48, v0
	v_lshlrev_b32_e32 v4, 2, v0
	v_rcp_iflag_f32_e32 v6, v6
	v_lshlrev_b32_e32 v5, 6, v0
	v_bfe_u32 v169, v0, 3, 3
	v_and_b32_e32 v0, 7, v0
	s_abs_i32 s57, s33
	v_lshlrev_b32_e32 v170, 4, v0
	v_add_lshl_u32 v171, v0, s10, 4
	v_mul_f32_e32 v0, 0x4f7ffffe, v6
	v_cvt_f32_u32_e32 v6, s57
	s_movk_i32 s0, 0x3c0
	s_mulk_i32 s20, 0x900
	v_cvt_u32_f32_e32 v0, v0
	v_rcp_iflag_f32_e32 v6, v6
	v_and_or_b32 v5, v5, s0, v2
	s_add_i32 s0, s20, 0
	v_lshl_or_b32 v3, v167, 6, v2
	v_and_b32_e32 v4, 32, v4
	s_add_i32 s0, s0, 0x20000
	v_bitop3_b32 v3, v3, s21, v4 bitop3:0xde
	v_bitop3_b32 v168, s23, v5, v4 bitop3:0xf6
	s_movk_i32 s1, 0x90
	v_mov_b32_e32 v4, s0
	v_mad_u32_u24 v5, v167, s1, v4
	v_mad_u32_u24 v4, v169, s1, v4
	v_readfirstlane_b32 s1, v0
	v_mul_f32_e32 v0, 0x4f7ffffe, v6
	v_cvt_u32_f32_e32 v0, v0
	s_sub_i32 s0, 0, s54
	s_mul_i32 s0, s0, s1
	s_mul_hi_u32 s0, s1, s0
	s_add_i32 s59, s1, s0
	s_sub_i32 s0, 0, s57
	v_readfirstlane_b32 s1, v0
	s_waitcnt vmcnt(6)
	s_mul_i32 s0, s0, s1
	v_add_u16_e32 v0, v1, v10
	s_mul_hi_u32 s0, s1, s0
	v_lshrrev_b16_e32 v0, 1, v0
	s_add_i32 s65, 0, 0x10000
	s_add_i32 s66, 0, 0x14000
	s_mov_b32 s23, 0x20000
	s_lshl_b32 s51, s22, 6
	s_waitcnt lgkmcnt(0)
	s_ashr_i32 s52, s11, 31
	s_lshl_b32 s22, s10, 17
	s_and_b32 s21, s9, 0xffff
	s_mov_b32 s20, s8
	s_lshl_b32 s55, s10, 5
	s_mul_i32 s56, s10, 48
	s_bfe_i32 s58, s33, 0x1001c
	s_ashr_i32 s60, s33, 31
	s_add_i32 s61, s1, s0
	s_mul_i32 s62, s10, 0xc0
	s_mul_i32 s63, s10, 0x60
	s_lshl_b32 s64, s10, 4
	v_add_lshl_u32 v152, v11, v0, 1
	v_mov_b32_e32 v153, v147
	v_add_lshl_u32 v154, v12, v0, 1
	v_mov_b32_e32 v155, v147
	v_mov_b64_e32 v[156:157], s[6:7]
	v_add_u32_e32 v172, s65, v168
	v_add_u32_e32 v173, 0, v3
	v_add_u32_e32 v174, s66, v168
	v_add_u32_e32 v175, v5, v2
	v_add_u32_e32 v176, v4, v170
	s_barrier

.LBB9_17:
	s_ashr_i32 s8, s34, 3
	s_add_i32 s34, s67, s8
	s_mov_b64 s[8:9], -1
	s_mov_b64 vcc, s[4:5]
	s_cbranch_vccz .LBB9_19
	s_abs_i32 s9, s34
	s_mul_hi_u32 s35, s9, s59
	s_mul_i32 s67, s35, s54
	s_ashr_i32 s8, s34, 31
	s_sub_i32 s9, s9, s67
	s_xor_b32 s8, s8, s58
	s_add_i32 s67, s35, 1
	s_sub_i32 s69, s9, s54
	s_cmp_ge_u32 s9, s54
	s_cselect_b32 s35, s67, s35
	s_cselect_b32 s9, s69, s9
	s_add_i32 s67, s35, 1
	s_cmp_ge_u32 s9, s54
	s_cselect_b32 s9, s67, s35
	s_xor_b32 s9, s9, s8
	s_sub_i32 s8, s9, s8
	s_lshl_b32 s9, s8, 1
	s_sub_i32 s35, s3, s9
	s_min_i32 s35, s35, 2
	s_abs_i32 s67, s35
	v_cvt_f32_u32_e32 v0, s67
	s_sub_i32 s72, 0, s67
	s_mul_i32 s8, s8, s53
	s_sub_i32 s8, s34, s8
	v_rcp_iflag_f32_e32 v0, v0
	s_abs_i32 s71, s8
	s_xor_b32 s69, s8, s35
	s_ashr_i32 s69, s69, 31
	v_mul_f32_e32 v0, 0x4f7ffffe, v0
	v_cvt_u32_f32_e32 v0, v0
	s_nop 0
	v_readfirstlane_b32 s73, v0
	s_mul_i32 s72, s72, s73
	s_mul_hi_u32 s72, s73, s72
	s_add_i32 s73, s73, s72
	s_mul_hi_u32 s72, s71, s73
	s_mul_i32 s73, s72, s67
	s_sub_i32 s71, s71, s73
	s_add_i32 s73, s72, 1
	s_sub_i32 s74, s71, s67
	s_cmp_ge_u32 s71, s67
	s_cselect_b32 s72, s73, s72
	s_cselect_b32 s71, s74, s71
	s_add_i32 s73, s72, 1
	s_cmp_ge_u32 s71, s67
	s_cselect_b32 s67, s73, s72
	s_xor_b32 s67, s67, s69
	s_sub_i32 s67, s67, s69
	s_mul_i32 s35, s67, s35
	s_sub_i32 s8, s8, s35
	s_add_i32 s35, s8, s9
	s_mov_b64 s[8:9], 0
